# attn loop2: A flushed as 256-B row segments (each wave stores 16 rows x 64 cols from both key-half staging tiles, double-buffered staging)
# baseline (speedup 1.0000x reference)
.Ll1_cont:
	ds_bpermute_b32 v2, v69, v84
	ds_bpermute_b32 v5, v69, v83
	v_max_f32_e32 v4, v84, v84
	v_max_f32_e32 v7, v83, v83
	ds_bpermute_b32 v3, v69, v63
	s_waitcnt lgkmcnt(2)
	v_max_f32_e32 v6, v2, v2
	v_max_f32_e32 v4, v4, v6
	v_sub_f32_e32 v6, v84, v4
	v_exp_f32_e32 v9, v6
	s_waitcnt lgkmcnt(1)
	v_max_f32_e32 v6, v5, v5
	v_sub_f32_e32 v2, v2, v4
	v_max_f32_e32 v6, v7, v6
	v_exp_f32_e32 v11, v2
	ds_bpermute_b32 v2, v69, v62
	v_sub_f32_e32 v5, v5, v6
	v_sub_f32_e32 v7, v83, v6
	v_exp_f32_e32 v10, v5
	v_exp_f32_e32 v8, v7
	v_cmp_gt_u32_e32 vcc, 32, v98
	s_waitcnt lgkmcnt(0)
	v_pk_mul_f32 v[2:3], v[10:11], v[2:3]
	s_nop 0
	v_pk_fma_f32 v[8:9], v[62:63], v[8:9], v[2:3]
	v_lshlrev_b32_e32 v2, 7, v184
	v_or3_b32 v10, v183, v2, v1
	s_and_saveexec_b64 s[0:1], vcc
	v_lshl_add_u32 v2, v10, 4, 0
	v_add_u32_e32 v2, 0x21000, v2
	v_mov_b32_e32 v5, v9
	v_mov_b32_e32 v7, v8
	ds_write_b128 v2, v[4:7]
	s_or_b64 exec, exec, s[0:1]
	s_lshl_b32 s12, s21, 7
	s_mov_b32 s3, 0
	v_or_b32_e32 v2, s12, v82
	s_lshl_b32 s13, s21, 11
	s_add_i32 s23, 0, 0x12000
	v_lshlrev_b32_e32 v2, 12, v2
	v_mov_b32_e32 v3, 0
	s_add_i32 s13, s13, s16
	s_lshl_b64 s[0:1], s[2:3], 13
	v_lshl_add_u64 v[12:13], s[14:15], 0, v[2:3]
	v_mov_b32_e32 v69, v3
	s_add_u32 s0, s10, s0
	v_lshl_add_u64 v[172:173], v[12:13], 0, v[68:69]
	s_addc_u32 s1, s11, s1
	s_lshl_b32 s10, s22, 7
	s_mov_b32 s11, s3
	s_waitcnt vmcnt(1)
	v_lshl_add_u64 v[36:37], v[172:173], 0, s[10:11]
	s_mov_b32 s10, 0x40000
	v_add_co_u32_e32 v38, vcc, s10, v36
	s_waitcnt lgkmcnt(0)
	s_barrier
	global_load_dwordx4 v[12:15], v[58:59], off
	global_load_dwordx4 v[16:19], v[70:71], off
	v_addc_co_u32_e32 v39, vcc, 0, v37, vcc
	global_load_dwordx4 v[20:23], v[56:57], off
	global_load_dwordx4 v[24:27], v[66:67], off
	global_load_dwordx4 v[28:31], v[36:37], off
	global_load_dwordx4 v[32:35], v[38:39], off
	v_add_f32_e32 v2, v78, v80
	s_movk_i32 s11, 0x1200
	v_add_f32_e32 v5, v79, v81
	s_mov_b32 s14, 0x3fb8aa3b
	v_lshlrev_b32_e32 v10, 4, v10
	v_mov_b32_e32 v36, s23
	v_mul_f32_e32 v37, 0x3fb8aa3b, v2
	v_mul_f32_e32 v38, 0x3fb8aa3b, v5
	v_xor_b32_e32 v10, 0x800, v10
	v_mad_u32_u24 v40, v55, s11, v36
	v_fma_f32 v36, v2, s14, -v37
	v_rndne_f32_e32 v39, v37
	v_fma_f32 v41, v5, s14, -v38
	s_waitcnt vmcnt(6)
	v_rndne_f32_e32 v42, v38
	v_add_u32_e32 v10, 0, v10
	v_fmac_f32_e32 v36, 0x32a5705f, v2
	v_sub_f32_e32 v37, v37, v39
	v_fmac_f32_e32 v41, 0x32a5705f, v5
	v_sub_f32_e32 v38, v38, v42
	v_add_u32_e32 v10, 0x21000, v10
	v_add_f32_e32 v44, v37, v36
	global_load_dwordx4 v[146:149], v[60:61], off
	global_load_dwordx4 v[150:153], v[64:65], off
	v_cvt_i32_f32_e32 v43, v39
	v_add_f32_e32 v41, v38, v41
	ds_read_b128 v[36:39], v10
	v_exp_f32_e32 v10, v44
	v_cvt_i32_f32_e32 v42, v42
	v_exp_f32_e32 v41, v41
	s_mov_b32 s21, 0xc2ce8ed0
	s_lshl_b32 s11, s20, 6
	s_add_i32 s14, s11, 64
	v_ldexp_f32 v10, v10, v43
	v_cmp_ngt_f32_e32 vcc, s21, v2
	s_mov_b32 s22, 0x42b17218
	s_and_b32 s14, s14, 0x7c0
	v_ldexp_f32 v41, v41, v42
	v_cndmask_b32_e32 v10, 0, v10, vcc
	v_cmp_ngt_f32_e32 vcc, s21, v5
	v_mov_b32_e32 v7, 0x7f800000
	v_max_f32_e32 v11, v4, v4
	s_mov_b32 s15, s3
	s_lshl_b32 s14, s14, 1
	s_waitcnt lgkmcnt(0)
	v_max_f32_e32 v42, v36, v36
	v_cndmask_b32_e32 v41, 0, v41, vcc
	v_cmp_nlt_f32_e32 vcc, s22, v2
	v_max_f32_e32 v187, v11, v42
	v_mov_b32_e32 v55, v3
	v_cndmask_b32_e32 v2, v7, v10, vcc
	v_cmp_nlt_f32_e32 vcc, s22, v5
	v_lshl_add_u64 v[10:11], v[172:173], 0, s[14:15]
	v_lshl_add_u64 v[178:179], s[0:1], 0, v[54:55]
	v_cndmask_b32_e32 v5, v7, v41, vcc
	v_sub_f32_e32 v2, v2, v5
	v_add_f32_e32 v41, 0x3e4ccccd, v2
	v_sub_f32_e32 v2, v4, v187
	v_max_f32_e32 v4, v6, v6
	s_and_b32 s1, s2, 7
	s_mulk_i32 s1, 0x280
	s_mulk_i32 s19, 0x140
	s_add_i32 s0, s20, 2
	s_waitcnt vmcnt(7)
	ds_write_b128 v185, v[12:15]
	s_waitcnt vmcnt(6)
	ds_write_b128 v185, v[16:19] offset:9216
	s_waitcnt vmcnt(5)
	ds_write_b128 v185, v[20:23] offset:18432
	s_waitcnt vmcnt(4)
	ds_write_b128 v185, v[24:27] offset:27648
	s_waitcnt vmcnt(3)
	ds_write_b128 v185, v[28:31] offset:36864
	s_waitcnt vmcnt(2)
	ds_write_b128 v185, v[32:35] offset:46080
	v_add_co_u32_e32 v12, vcc, s10, v10
	v_exp_f32_e32 v23, v2
	s_nop 0
	v_addc_co_u32_e32 v13, vcc, 0, v11, vcc
	global_load_dwordx4 v[154:157], v[10:11], off
	global_load_dwordx4 v[158:161], v[12:13], off
	s_waitcnt lgkmcnt(0)
	s_barrier
	ds_read_b128 v[10:13], v186
	v_sub_f32_e32 v2, v36, v187
	v_exp_f32_e32 v25, v2
	v_max_f32_e32 v2, v38, v38
	v_max_f32_e32 v188, v4, v2
	v_sub_f32_e32 v2, v6, v188
	v_exp_f32_e32 v22, v2
	v_sub_f32_e32 v2, v38, v188
	v_exp_f32_e32 v24, v2
	ds_read_b128 v[14:17], v186 offset:9216
	ds_read_b128 v[18:21], v186 offset:32
	s_waitcnt lgkmcnt(2)
	v_mfma_f32_32x32x16_f16 v[66:81], v[10:13], v[114:117], 0
	v_mov_b32_e32 v36, v39
	v_mul_f32_e64 v10, v36, v24
	v_mul_f32_e64 v11, v37, v25
	ds_read_b128 v[4:7], v186 offset:9248
	s_add_i32 s1, s1, s19
	s_mov_b32 s14, 0x18000
	s_mov_b32 s15, 0x80000
	s_mov_b32 s19, 0
	s_waitcnt lgkmcnt(2)
	v_mfma_f32_32x32x16_f16 v[82:97], v[14:17], v[130:133], 0
	v_fma_f32 v16, v8, v22, v10
	v_fma_f32 v17, v9, v23, v11
	v_log_f32_e32 v238, v17
	s_nop 0
	v_add_f32_e32 v187, v187, v238
	v_sub_f32_e32 v240, 0, v187
	v_sub_f32_e32 v241, 0, v187
	v_sub_f32_e32 v242, 0, v187
	v_sub_f32_e32 v243, 0, v187
	v_sub_f32_e32 v244, 0, v187
	v_sub_f32_e32 v245, 0, v187
	v_sub_f32_e32 v246, 0, v187
	v_sub_f32_e32 v247, 0, v187
	v_sub_f32_e32 v248, 0, v187
	v_sub_f32_e32 v249, 0, v187
	v_sub_f32_e32 v250, 0, v187
	v_sub_f32_e32 v251, 0, v187
	v_sub_f32_e32 v252, 0, v187
	v_sub_f32_e32 v253, 0, v187
	v_sub_f32_e32 v254, 0, v187
	v_sub_f32_e32 v255, 0, v187
	v_lshrrev_b32_e32 v22, 3, v98
	v_lshrrev_b32_e32 v22, 4, v98
	v_lshl_or_b32 v22, v184, 4, v22
	v_or3_b32 v2, s13, v183, v22
	v_lshlrev_b64 v[8:9], 13, v[2:3]
	v_lshl_add_u64 v[8:9], s[4:5], 0, v[8:9]
	v_mov_b32_e32 v2, 0
	v_lshl_add_u64 v[8:9], v[8:9], 0, v[2:3]
	v_and_b32_e32 v2, 0xf0, v54
	v_lshl_add_u64 v[174:175], v[8:9], 0, v[2:3]
	ds_read_b128 v[8:11], v186 offset:64
	s_waitcnt lgkmcnt(2)
	v_mfma_f32_32x32x16_f16 v[66:81], v[18:21], v[118:121], v[66:81]
	v_div_scale_f32 v18, s[4:5], v16, v16, -v41
	v_rcp_f32_e32 v19, v18
	v_div_scale_f32 v20, vcc, -v41, v16, -v41
	s_mov_b32 s13, 0x10000
	v_mov_b32_e32 v24, v3
	s_waitcnt lgkmcnt(1)
	v_mfma_f32_32x32x16_f16 v[82:97], v[4:7], v[134:137], v[82:97]
	v_fma_f32 v4, -v18, v19, 1.0
	v_fmac_f32_e32 v19, v4, v19
	v_mul_f32_e32 v21, v20, v19
	ds_read_b128 v[4:7], v186 offset:9280
	ds_read_b128 v[12:15], v186 offset:96
	v_mov_b32_e32 v25, v3
	v_mov_b32_e32 v26, v3
	v_mov_b32_e32 v27, v3
	s_waitcnt lgkmcnt(2)
	v_mfma_f32_32x32x16_f16 v[66:81], v[8:11], v[122:125], v[66:81]
	v_fma_f32 v8, -v18, v21, v20
	v_fmac_f32_e32 v21, v8, v19
	v_fma_f32 v18, -v18, v21, v20
	v_div_scale_f32 v20, s[4:5], v17, v17, 1.0
	v_rcp_f32_e32 v23, v20
	ds_read_b128 v[8:11], v186 offset:9312
	s_waitcnt lgkmcnt(2)
	v_mfma_f32_32x32x16_f16 v[82:97], v[4:7], v[138:141], v[82:97]
	v_div_fmas_f32 v4, v18, v19, v21
	v_div_fixup_f32 v176, v4, v16, -v41
	v_fma_f32 v4, -v20, v23, 1.0
	v_fmac_f32_e32 v23, v4, v23
	v_div_scale_f32 v4, vcc, 1.0, v17, 1.0
	v_mul_f32_e32 v5, v4, v23
	v_fma_f32 v6, -v20, v5, v4
	v_fmac_f32_e32 v5, v6, v23
	s_waitcnt lgkmcnt(1)
	v_mfma_f32_32x32x16_f16 v[66:81], v[12:15], v[126:129], v[66:81]
	v_fma_f32 v4, -v20, v5, v4
	v_div_fmas_f32 v4, v4, v23, v5
	v_div_fixup_f32 v177, v4, v17, 1.0
	v_mul_u32_u24_e32 v4, 0x90, v22
	v_lshrrev_b32_e32 v98, 6, v0
	v_and_b32_e32 v189, 3, v98
	v_mul_u32_u24_e32 v189, 0x1200, v189
	v_lshrrev_b32_e32 v98, 2, v98
	v_lshlrev_b32_e32 v98, 4, v98
	v_bfe_u32 v4, v0, 4, 2
	v_add_u32_e32 v98, v98, v4
	v_mul_u32_u24_e32 v98, 0x90, v98
	v_add_u32_e32 v189, v189, v98
	v_bfe_u32 v4, v0, 3, 1
	v_mul_u32_u24_e32 v4, 0x4800, v4
	v_add_u32_e32 v189, v189, v4
	v_and_b32_e32 v4, 7, v0
	v_lshl_add_u32 v189, v4, 4, v189
	v_add_u32_e32 v189, 0x12000, v189
	v_and_b32_e32 v98, 63, v0
	v_mul_u32_u24_e32 v2, 0x90, v1
	v_lshlrev_b32_e32 v4, 2, v99
	s_waitcnt lgkmcnt(0)
	v_mfma_f32_32x32x16_f16 v[82:97], v[8:11], v[142:145], v[82:97]
	v_add3_u32 v190, v40, v2, v4
	v_mul_u32_u24_e32 v2, 0x48, v1
	v_lshl_add_u32 v2, v2, 1, 0
	v_lshlrev_b32_e32 v4, 1, v101
	v_add3_u32 v191, v2, v4, v100
	s_mov_b32 s4, 0x3f800000
	s_mov_b32 s5, 0x8000
	v_mov_b32_e32 v2, v3
	v_mov_b32_e32 v4, v3
	v_mov_b32_e32 v5, v3
	v_mov_b32_e32 v6, v3
	v_mov_b32_e32 v7, v3
	v_mov_b32_e32 v8, v3
	v_mov_b32_e32 v9, v3
	v_mov_b32_e32 v10, v3
	v_mov_b32_e32 v11, v3
	v_mov_b32_e32 v12, v3
	v_mov_b32_e32 v13, v3
	v_mov_b32_e32 v14, v3
	v_mov_b32_e32 v15, v3
	v_mov_b32_e32 v16, v3
	v_mov_b32_e32 v17, v3
	v_mov_b32_e32 v18, v3
	v_mov_b32_e32 v19, v3
	v_mov_b32_e32 v20, v3
	v_mov_b32_e32 v21, v3
	v_mov_b32_e32 v22, v3
	v_mov_b32_e32 v23, v3
	v_mov_b32_e32 v28, v3
	v_mov_b32_e32 v29, v3
	v_mov_b32_e32 v30, v3
	v_mov_b32_e32 v31, v3
	v_mov_b32_e32 v32, v3
	v_mov_b32_e32 v33, v3
	v_mov_b32_e32 v34, v3
	v_mov_b32_e32 v35, v3
	v_mov_b32_e32 v36, v3
	v_mov_b32_e32 v37, v3
	v_mov_b32_e32 v38, v3
	v_mov_b32_e32 v39, v3
	v_mov_b32_e32 v40, v3
	v_mov_b32_e32 v41, v3
	v_mov_b32_e32 v42, v3
	v_mov_b32_e32 v43, v3
	v_mov_b32_e32 v44, v3
	v_mov_b32_e32 v45, v3
	v_mov_b32_e32 v46, v3
	v_mov_b32_e32 v47, v3
	v_mov_b32_e32 v48, v3
	v_mov_b32_e32 v49, v3
	v_mov_b32_e32 v50, v3
	v_mov_b32_e32 v51, v3
	v_mov_b32_e32 v52, v3
	v_mov_b32_e32 v53, v3
	v_mov_b32_e32 v54, v3
	v_mov_b32_e32 v56, v3
	v_mov_b32_e32 v57, v3
	v_mov_b32_e32 v58, v3
	v_mov_b32_e32 v59, v3
	v_mov_b32_e32 v60, v3
	v_mov_b32_e32 v61, v3
	v_mov_b32_e32 v62, v3
	v_mov_b32_e32 v63, v3
	v_mov_b32_e32 v64, v3
	v_mov_b32_e32 v65, v3
	v_add_u32_e32 v192, 0xd800, v191
	v_sub_f32_e32 v66, v66, v187
	v_sub_f32_e32 v67, v67, v187
	v_sub_f32_e32 v68, v68, v187
	v_sub_f32_e32 v69, v69, v187
	v_sub_f32_e32 v70, v70, v187
	v_sub_f32_e32 v71, v71, v187
	v_sub_f32_e32 v72, v72, v187
	v_sub_f32_e32 v73, v73, v187
	v_sub_f32_e32 v74, v74, v187
	v_sub_f32_e32 v75, v75, v187
	v_sub_f32_e32 v76, v76, v187
	v_sub_f32_e32 v77, v77, v187
	v_sub_f32_e32 v78, v78, v187
	v_sub_f32_e32 v79, v79, v187
	v_sub_f32_e32 v80, v80, v187
	v_sub_f32_e32 v81, v81, v187
	s_mov_b32 s27, 0x42c80000
	v_cmp_gt_f32_e64 vcc, |v188|, s27
	s_cbranch_vccnz .Ll2_gen
	v_sub_f32_e32 v238, 0, v188
	v_exp_f32_e32 v238, v238
	s_nop 0
	v_mul_f32_e32 v176, v176, v238
	s_barrier
	s_branch .Ll2f_top

.LBB4_7:
	v_exp_f32_e32 v215, v66
	s_nop 8
	v_fma_f32 v66, v82, s4, -v188
	v_exp_f32_e32 v216, v66
	v_exp_f32_e32 v217, v67
	v_fma_f32 v66, v83, s4, -v188
	v_exp_f32_e32 v214, v66
	v_exp_f32_e32 v219, v68
	v_fma_f32 v66, v84, s4, -v188
	v_exp_f32_e32 v220, v66
	ds_read_b128 v[98:101], v186 offset:18432
	ds_read_b128 v[162:165], v186 offset:18464
	ds_read_b128 v[194:197], v186 offset:27648
	ds_read_b128 v[198:201], v186 offset:27680
	ds_read_b128 v[202:205], v186 offset:18496
	ds_read_b128 v[206:209], v186 offset:18528
	ds_read_b128 v[210:213], v186 offset:27712
	ds_read_b128 v[166:169], v186 offset:27744
	v_exp_f32_e32 v221, v69
	v_fma_f32 v66, v85, s4, -v188
	v_exp_f32_e32 v218, v66
	s_waitcnt lgkmcnt(7)
	v_mfma_f32_32x32x16_f16 v[98:113], v[98:101], v[114:117], v[240:255]
	v_exp_f32_e32 v223, v70
	v_fma_f32 v66, v86, s4, -v188
	v_exp_f32_e32 v70, v66
	v_exp_f32_e32 v71, v71
	v_fma_f32 v66, v87, s4, -v188
	v_exp_f32_e32 v222, v66
	v_exp_f32_e32 v225, v72
	v_fma_f32 v66, v88, s4, -v188
	v_exp_f32_e32 v226, v66
	v_exp_f32_e32 v227, v73
	v_fma_f32 v66, v89, s4, -v188
	v_exp_f32_e32 v224, v66
	s_waitcnt lgkmcnt(6)
	v_mfma_f32_32x32x16_f16 v[98:113], v[162:165], v[118:121], v[98:113]
	v_exp_f32_e32 v229, v74
	v_fma_f32 v66, v90, s4, -v188
	v_exp_f32_e32 v230, v66
	v_exp_f32_e32 v231, v75
	v_fma_f32 v66, v91, s4, -v188
	v_exp_f32_e32 v228, v66
	v_exp_f32_e32 v233, v76
	v_fma_f32 v66, v92, s4, -v188
	v_exp_f32_e32 v234, v66
	v_exp_f32_e32 v235, v77
	v_fma_f32 v66, v93, s4, -v188
	v_exp_f32_e32 v232, v66
	s_waitcnt lgkmcnt(3)
	v_mfma_f32_32x32x16_f16 v[98:113], v[202:205], v[122:125], v[98:113]
	v_exp_f32_e32 v237, v78
	v_fma_f32 v66, v94, s4, -v188
	v_exp_f32_e32 v162, v66
	v_exp_f32_e32 v163, v79
	v_fma_f32 v66, v95, s4, -v188
	v_exp_f32_e32 v236, v66
	v_exp_f32_e32 v165, v80
	v_fma_f32 v66, v96, s4, -v188
	v_exp_f32_e32 v202, v66
	v_exp_f32_e32 v203, v81
	v_fma_f32 v66, v97, s4, -v188
	v_exp_f32_e32 v193, v66
	s_waitcnt lgkmcnt(2)
	v_mfma_f32_32x32x16_f16 v[98:113], v[206:209], v[126:129], v[98:113]
	s_waitcnt vmcnt(3)
	ds_write_b128 v185, v[146:149]
	s_waitcnt vmcnt(2)
	ds_write_b128 v185, v[150:153] offset:9216
	s_waitcnt vmcnt(1)
	ds_write_b128 v185, v[154:157] offset:55296
	s_waitcnt vmcnt(0)
	ds_write_b128 v185, v[158:161] offset:64512
	v_fma_f32 v150, v176, v216, v215
	v_fma_f32 v151, v176, v214, v217
	ds_read_b128 v[66:69], v189 offset:36864
	ds_read_b128 v[88:91], v189 offset:37440
	v_fma_f32 v152, v176, v220, v219
	v_fma_f32 v153, v176, v218, v221
	ds_read_b128 v[92:95], v189 offset:38016
	ds_read_b128 v[146:149], v189 offset:38592
	v_fma_f32 v154, v176, v70, v223
	v_fma_f32 v155, v176, v222, v71
	ds_write_b128 v190, v[150:153]
	v_fma_f32 v156, v176, v226, v225
	v_fma_f32 v157, v176, v224, v227
	ds_write_b128 v190, v[154:157] offset:16
	v_fma_f32 v158, v176, v230, v229
	v_fma_f32 v159, v176, v228, v231
	v_cvt_pk_f16_f32 v157, v156, v157
	v_fma_f32 v160, v176, v234, v233
	v_fma_f32 v161, v176, v232, v235
	ds_write_b128 v190, v[158:161] offset:64
	v_fma_f32 v162, v176, v162, v237
	v_fma_f32 v163, v176, v236, v163
	v_cvt_pk_f16_f32 v156, v154, v155
	v_fma_f32 v164, v176, v202, v165
	v_fma_f32 v165, v176, v193, v203
	ds_write_b128 v190, v[162:165] offset:80
	v_cvt_pk_f16_f32 v155, v152, v153
	v_cvt_pk_f16_f32 v154, v150, v151
	ds_read_b128 v[150:153], v191 offset:36864
	s_cmp_eq_u32 s19, 0
	s_cselect_b64 vcc, -1, 0
	s_add_i32 s20, s16, s1
	v_mfma_f32_32x32x16_f16 v[72:87], v[194:197], v[130:133], 0
	ds_read_b128 v[194:197], v191 offset:36896
	s_add_i32 s2, s20, 0x7c0
	s_and_b32 s2, s2, 0x7c0
	s_lshl_b32 s2, s2, 2
	v_lshl_add_u64 v[70:71], v[174:175], 0, s[2:3]
	v_cndmask_b32_e32 v71, v71, v179, vcc
	v_cndmask_b32_e32 v70, v70, v178, vcc
	s_waitcnt lgkmcnt(1)
	v_mfma_f32_32x32x16_f16 v[50:65], v[154:157], v[150:153], v[50:65]
	ds_read_b128 v[150:153], v191 offset:41472
	global_store_dwordx4 v[70:71], v[66:69], off nt
	ds_read_b128 v[66:69], v191 offset:41504
	v_cvt_pk_f16_f32 v165, v164, v165
	v_cvt_pk_f16_f32 v164, v162, v163
	v_cvt_pk_f16_f32 v163, v160, v161
	v_cvt_pk_f16_f32 v162, v158, v159
	s_waitcnt lgkmcnt(1)
	v_mfma_f32_32x32x16_f16 v[34:49], v[154:157], v[150:153], v[34:49]
	v_add_co_u32_e32 v96, vcc, s5, v70
	s_min_u32 s2, s19, 28
	s_nop 0
	v_addc_co_u32_e32 v97, vcc, 0, v71, vcc
	global_store_dwordx4 v[96:97], v[88:91], off nt
	s_add_i32 s21, s17, s2
	s_waitcnt lgkmcnt(0)
	v_mfma_f32_32x32x16_f16 v[34:49], v[162:165], v[66:69], v[34:49]
	ds_read_b128 v[66:69], v191 offset:46080
	v_add_co_u32_e32 v88, vcc, s13, v70
	s_lshl_b32 s2, s21, 13
	s_nop 0
	v_addc_co_u32_e32 v89, vcc, 0, v71, vcc
	global_store_dwordx4 v[88:89], v[92:95], off nt
	ds_read_b128 v[88:91], v191 offset:46112
	s_waitcnt lgkmcnt(1)
	v_mfma_f32_32x32x16_f16 v[18:33], v[154:157], v[66:69], v[18:33]
	v_add_co_u32_e32 v70, vcc, s14, v70
	s_and_b32 s2, s2, 0x3e000
	s_nop 0
	v_addc_co_u32_e32 v71, vcc, 0, v71, vcc
	v_lshl_add_u64 v[66:67], v[170:171], 0, s[2:3]
	v_add_co_u32_e32 v68, vcc, s15, v66
	global_store_dwordx4 v[70:71], v[146:149], off nt
	s_nop 0
	v_addc_co_u32_e32 v69, vcc, 0, v67, vcc
	s_waitcnt lgkmcnt(0)
	v_mfma_f32_32x32x16_f16 v[18:33], v[162:165], v[88:91], v[18:33]
	global_load_dwordx4 v[88:91], v[66:67], off
	global_load_dwordx4 v[92:95], v[68:69], off
	ds_read_b128 v[66:69], v191 offset:50688
	ds_read_b128 v[146:149], v191 offset:50720
	s_min_u32 s2, s19, 29
	s_add_i32 s2, s0, s2
	s_lshl_b32 s2, s2, 7
	s_and_b32 s2, s2, 0xf80
	s_waitcnt lgkmcnt(1)
	v_mfma_f32_32x32x16_f16 v[2:17], v[154:157], v[66:69], v[2:17]
	v_lshl_add_u64 v[66:67], v[172:173], 0, s[2:3]
	v_add_co_u32_e32 v68, vcc, s10, v66
	s_nop 0
	v_addc_co_u32_e32 v69, vcc, 0, v67, vcc
	global_load_dwordx4 v[150:153], v[66:67], off
	global_load_dwordx4 v[154:157], v[68:69], off
	v_mfma_f32_32x32x16_f16 v[72:87], v[198:201], v[134:137], v[72:87]
	v_exp_f32_e32 v97, v98
	s_waitcnt lgkmcnt(0)
	s_barrier
	v_mfma_f32_32x32x16_f16 v[72:87], v[210:213], v[138:141], v[72:87]
	v_mfma_f32_32x32x16_f16 v[72:87], v[166:169], v[142:145], v[72:87]
	v_mfma_f32_32x32x16_f16 v[50:65], v[162:165], v[194:197], v[50:65]
	s_nop 10
	v_fma_f32 v70, v72, s4, -v188
	v_exp_f32_e32 v166, v70
	v_exp_f32_e32 v167, v99
	v_fma_f32 v70, v73, s4, -v188
	v_exp_f32_e32 v96, v70
	v_exp_f32_e32 v99, v100
	v_fma_f32 v70, v74, s4, -v188
	v_exp_f32_e32 v168, v70
	v_exp_f32_e32 v169, v101
	v_fma_f32 v70, v75, s4, -v188
	v_exp_f32_e32 v98, v70
	v_exp_f32_e32 v101, v102
	v_fma_f32 v70, v76, s4, -v188
	v_exp_f32_e32 v210, v70
	v_exp_f32_e32 v211, v103
	v_fma_f32 v70, v77, s4, -v188
	v_exp_f32_e32 v100, v70
	v_exp_f32_e32 v103, v104
	v_fma_f32 v70, v78, s4, -v188
	v_exp_f32_e32 v212, v70
	v_exp_f32_e32 v213, v105
	v_fma_f32 v70, v79, s4, -v188
	v_exp_f32_e32 v102, v70
	v_exp_f32_e32 v105, v106
	v_fma_f32 v70, v80, s4, -v188
	v_exp_f32_e32 v214, v70
	v_exp_f32_e32 v215, v107
	v_fma_f32 v70, v81, s4, -v188
	v_mfma_f32_32x32x16_f16 v[2:17], v[162:165], v[146:149], v[2:17]
	ds_read_b128 v[66:69], v186
	ds_read_b128 v[158:161], v186 offset:32
	ds_read_b128 v[194:197], v186 offset:9216
	ds_read_b128 v[198:201], v186 offset:9248
	ds_read_b128 v[202:205], v186 offset:64
	ds_read_b128 v[206:209], v186 offset:96
	ds_read_b128 v[146:149], v186 offset:9280
	ds_read_b128 v[162:165], v186 offset:9312
	v_exp_f32_e32 v104, v70
	v_exp_f32_e32 v107, v108
	v_fma_f32 v82, v82, s4, -v188
	v_exp_f32_e32 v216, v82
	s_waitcnt lgkmcnt(7)
	v_mfma_f32_32x32x16_f16 v[66:81], v[66:69], v[114:117], v[240:255]
	v_exp_f32_e32 v217, v109
	v_fma_f32 v82, v83, s4, -v188
	v_exp_f32_e32 v106, v82
	v_exp_f32_e32 v109, v110
	v_fma_f32 v82, v84, s4, -v188
	v_exp_f32_e32 v218, v82
	s_waitcnt lgkmcnt(6)
	v_mfma_f32_32x32x16_f16 v[66:81], v[158:161], v[118:121], v[66:81]
	v_exp_f32_e32 v219, v111
	v_fma_f32 v82, v85, s4, -v188
	v_exp_f32_e32 v108, v82
	v_exp_f32_e32 v111, v112
	v_fma_f32 v82, v86, s4, -v188
	s_waitcnt lgkmcnt(3)
	v_mfma_f32_32x32x16_f16 v[66:81], v[202:205], v[122:125], v[66:81]
	v_exp_f32_e32 v202, v82
	v_exp_f32_e32 v203, v113
	v_fma_f32 v82, v87, s4, -v188
	v_exp_f32_e32 v110, v82
	s_waitcnt lgkmcnt(2)
	v_mfma_f32_32x32x16_f16 v[66:81], v[206:209], v[126:129], v[66:81]
	s_waitcnt vmcnt(3)
	ds_write_b128 v185, v[88:91] offset:18432
	s_waitcnt vmcnt(2)
	ds_write_b128 v185, v[92:95] offset:27648
	s_waitcnt vmcnt(1)
	ds_write_b128 v185, v[150:153] offset:36864
	s_waitcnt vmcnt(0)
	ds_write_b128 v185, v[154:157] offset:46080
	v_fma_f32 v150, v176, v166, v97
	v_fma_f32 v151, v176, v96, v167
	v_mfma_f32_32x32x16_f16 v[82:97], v[194:197], v[130:133], 0
	v_fma_f32 v152, v176, v168, v99
	v_fma_f32 v153, v176, v98, v169
	v_fma_f32 v154, v176, v210, v101
	v_fma_f32 v155, v176, v100, v211
	v_fma_f32 v156, v176, v212, v103
	v_fma_f32 v157, v176, v102, v213
	v_fma_f32 v158, v176, v214, v105
	v_fma_f32 v159, v176, v104, v215
	v_fma_f32 v160, v176, v216, v107
	v_fma_f32 v161, v176, v106, v217
	v_fma_f32 v166, v176, v218, v109
	v_fma_f32 v167, v176, v108, v219
	v_fma_f32 v168, v176, v202, v111
	v_fma_f32 v169, v176, v110, v203
	ds_read_b128 v[98:101], v189
	ds_read_b128 v[102:105], v189 offset:576
	ds_read_b128 v[106:109], v189 offset:1152
	ds_read_b128 v[110:113], v189 offset:1728
	ds_write_b128 v190, v[150:153] offset:36864
	ds_write_b128 v190, v[154:157] offset:36880
	ds_write_b128 v190, v[158:161] offset:36928
	ds_write_b128 v190, v[166:169] offset:36944
	v_cvt_pk_f16_f32 v157, v156, v157
	v_cvt_pk_f16_f32 v156, v154, v155
	v_cvt_pk_f16_f32 v155, v152, v153
	v_cvt_pk_f16_f32 v154, v150, v151
	ds_read_b128 v[150:153], v191 offset:55296
	ds_read_b128 v[194:197], v191 offset:55328
	v_mfma_f32_32x32x16_f16 v[82:97], v[198:201], v[134:137], v[82:97]
	s_and_b32 s2, s20, 0x7c0
	s_min_u32 s20, s19, 27
	s_lshl_b32 s2, s2, 2
	s_add_i32 s20, s18, s20
	v_lshl_add_u64 v[210:211], v[174:175], 0, s[2:3]
	s_lshl_b32 s2, s20, 13
	s_and_b32 s2, s2, 0x3e000
	s_waitcnt lgkmcnt(1)
	v_mfma_f32_32x32x16_f16 v[50:65], v[154:157], v[150:153], v[50:65]
	ds_read_b128 v[150:153], v191 offset:59904
	ds_read_b128 v[198:201], v191 offset:59936
	s_lshl_b32 s21, s21, 7
	v_cvt_pk_f16_f32 v169, v168, v169
	v_cvt_pk_f16_f32 v168, v166, v167
	v_cvt_pk_f16_f32 v166, v158, v159
	v_cvt_pk_f16_f32 v167, v160, v161
	s_addk_i32 s1, 0x80
	s_waitcnt lgkmcnt(1)
	v_mfma_f32_32x32x16_f16 v[34:49], v[154:157], v[150:153], v[34:49]
	ds_read_b128 v[150:153], v191 offset:64512
	ds_read_b128 v[202:205], v191 offset:64544
	s_waitcnt lgkmcnt(1)
	v_mfma_f32_32x32x16_f16 v[18:33], v[154:157], v[150:153], v[18:33]
	ds_read_b128 v[150:153], v192 offset:13824
	ds_read_b128 v[206:209], v192 offset:13856
	v_mfma_f32_32x32x16_f16 v[82:97], v[146:149], v[138:141], v[82:97]
	v_lshl_add_u64 v[146:147], v[170:171], 0, s[2:3]
	s_and_b32 s2, s21, 0xf80
	v_lshl_add_u64 v[158:159], v[172:173], 0, s[2:3]
	s_add_i32 s2, s19, 2
	s_cmp_lt_u32 s19, 30
	s_mov_b32 s19, s2
	s_waitcnt lgkmcnt(1)
	v_mfma_f32_32x32x16_f16 v[2:17], v[154:157], v[150:153], v[2:17]
	v_add_co_u32_e32 v150, vcc, s15, v146
	s_nop 1
	v_addc_co_u32_e32 v151, vcc, 0, v147, vcc
	global_load_dwordx4 v[146:149], v[146:147], off
	s_nop 0
	global_load_dwordx4 v[150:153], v[150:151], off
	s_nop 0
	global_load_dwordx4 v[154:157], v[158:159], off
	v_add_co_u32_e32 v158, vcc, s10, v158
	v_mfma_f32_32x32x16_f16 v[50:65], v[166:169], v[194:197], v[50:65]
	s_nop 0
	v_addc_co_u32_e32 v159, vcc, 0, v159, vcc
	global_load_dwordx4 v[158:161], v[158:159], off
	v_add_co_u32_e32 v194, vcc, s5, v210
	s_nop 1
	v_addc_co_u32_e32 v195, vcc, 0, v211, vcc
	v_mfma_f32_32x32x16_f16 v[34:49], v[166:169], v[198:201], v[34:49]
	v_add_co_u32_e32 v196, vcc, s13, v210
	s_nop 1
	v_addc_co_u32_e32 v197, vcc, 0, v211, vcc
	v_mfma_f32_32x32x16_f16 v[18:33], v[166:169], v[202:205], v[18:33]
	s_waitcnt lgkmcnt(0)
	v_mfma_f32_32x32x16_f16 v[2:17], v[166:169], v[206:209], v[2:17]
	v_add_co_u32_e32 v166, vcc, s14, v210
	s_nop 1
	v_addc_co_u32_e32 v167, vcc, 0, v211, vcc
	global_store_dwordx4 v[210:211], v[98:101], off nt
	global_store_dwordx4 v[194:195], v[102:105], off nt
	global_store_dwordx4 v[196:197], v[106:109], off nt
	global_store_dwordx4 v[166:167], v[110:113], off nt
	v_mfma_f32_32x32x16_f16 v[82:97], v[162:165], v[142:145], v[82:97]
	s_barrier
	s_cbranch_scc1 .LBB4_7
	s_branch .Ll2_post
	.p2alignl 6, 3212836864
	s_nop 0
	s_nop 0
	s_nop 0
	s_nop 0
.Ll2f_top:
	ds_read_b128 v[98:101], v186 offset:18432
	ds_read_b128 v[162:165], v186 offset:18464
	ds_read_b128 v[194:197], v186 offset:27648
	ds_read_b128 v[198:201], v186 offset:27680
	ds_read_b128 v[202:205], v186 offset:18496
	ds_read_b128 v[206:209], v186 offset:18528
	ds_read_b128 v[210:213], v186 offset:27712
	ds_read_b128 v[166:169], v186 offset:27744
	s_nop 0
	v_exp_f32_e32 v215, v66
	v_exp_f32_e32 v217, v67
	v_exp_f32_e32 v219, v68
	v_exp_f32_e32 v221, v69
	v_exp_f32_e32 v223, v70
	v_exp_f32_e32 v71, v71
	v_exp_f32_e32 v225, v72
	v_exp_f32_e32 v227, v73
	v_exp_f32_e32 v229, v74
	v_exp_f32_e32 v231, v75
	s_waitcnt lgkmcnt(7)
	v_mfma_f32_32x32x16_f16 v[98:113], v[98:101], v[114:117], v[240:255]
	v_exp_f32_e32 v216, v82
	v_exp_f32_e32 v214, v83
	v_exp_f32_e32 v220, v84
	v_exp_f32_e32 v218, v85
	v_exp_f32_e32 v70, v86
	v_exp_f32_e32 v222, v87
	v_exp_f32_e32 v226, v88
	v_exp_f32_e32 v224, v89
	s_waitcnt lgkmcnt(6)
	v_mfma_f32_32x32x16_f16 v[98:113], v[162:165], v[118:121], v[98:113]
	v_exp_f32_e32 v233, v76
	v_exp_f32_e32 v235, v77
	v_exp_f32_e32 v230, v90
	v_exp_f32_e32 v228, v91
	v_exp_f32_e32 v234, v92
	v_exp_f32_e32 v232, v93
	v_exp_f32_e32 v237, v78
	v_exp_f32_e32 v236, v95
	s_waitcnt lgkmcnt(3)
	v_mfma_f32_32x32x16_f16 v[98:113], v[202:205], v[122:125], v[98:113]
	v_exp_f32_e32 v162, v94
	v_exp_f32_e32 v163, v79
	v_exp_f32_e32 v165, v80
	v_exp_f32_e32 v202, v96
	v_exp_f32_e32 v203, v81
	v_exp_f32_e32 v193, v97
	s_waitcnt lgkmcnt(2)
	v_mfma_f32_32x32x16_f16 v[98:113], v[206:209], v[126:129], v[98:113]
	s_waitcnt vmcnt(3)
	ds_write_b128 v185, v[146:149]
	s_waitcnt vmcnt(2)
	ds_write_b128 v185, v[150:153] offset:9216
	s_waitcnt vmcnt(1)
	ds_write_b128 v185, v[154:157] offset:55296
	s_waitcnt vmcnt(0)
	ds_write_b128 v185, v[158:161] offset:64512
	v_fma_f32 v150, v176, v216, v215
	v_fma_f32 v151, v176, v214, v217
	ds_read_b128 v[66:69], v189 offset:36864
	ds_read_b128 v[88:91], v189 offset:37440
	v_fma_f32 v152, v176, v220, v219
	v_fma_f32 v153, v176, v218, v221
	ds_read_b128 v[92:95], v189 offset:38016
	ds_read_b128 v[146:149], v189 offset:38592
	v_fma_f32 v154, v176, v70, v223
	v_fma_f32 v155, v176, v222, v71
	ds_write_b128 v190, v[150:153]
	v_fma_f32 v156, v176, v226, v225
	v_fma_f32 v157, v176, v224, v227
	ds_write_b128 v190, v[154:157] offset:16
	v_fma_f32 v158, v176, v230, v229
	v_fma_f32 v159, v176, v228, v231
	v_cvt_pk_f16_f32 v157, v156, v157
	v_fma_f32 v160, v176, v234, v233
	v_fma_f32 v161, v176, v232, v235
	ds_write_b128 v190, v[158:161] offset:64
	v_fma_f32 v162, v176, v162, v237
	v_fma_f32 v163, v176, v236, v163
	v_cvt_pk_f16_f32 v156, v154, v155
	v_fma_f32 v164, v176, v202, v165
	v_fma_f32 v165, v176, v193, v203
	ds_write_b128 v190, v[162:165] offset:80
	v_cvt_pk_f16_f32 v155, v152, v153
	v_cvt_pk_f16_f32 v154, v150, v151
	ds_read_b128 v[150:153], v191 offset:36864
	s_cmp_eq_u32 s19, 0
	s_cselect_b64 vcc, -1, 0
	s_add_i32 s20, s16, s1
	v_mfma_f32_32x32x16_f16 v[72:87], v[194:197], v[130:133], 0
	ds_read_b128 v[194:197], v191 offset:36896
	s_add_i32 s2, s20, 0x7c0
	s_and_b32 s2, s2, 0x7c0
	s_lshl_b32 s2, s2, 2
	v_lshl_add_u64 v[70:71], v[174:175], 0, s[2:3]
	v_cndmask_b32_e32 v71, v71, v179, vcc
	v_cndmask_b32_e32 v70, v70, v178, vcc
	s_waitcnt lgkmcnt(1)
	v_mfma_f32_32x32x16_f16 v[50:65], v[154:157], v[150:153], v[50:65]
	ds_read_b128 v[150:153], v191 offset:41472
	global_store_dwordx4 v[70:71], v[66:69], off nt
	ds_read_b128 v[66:69], v191 offset:41504
	v_cvt_pk_f16_f32 v165, v164, v165
	v_cvt_pk_f16_f32 v164, v162, v163
	v_cvt_pk_f16_f32 v163, v160, v161
	v_cvt_pk_f16_f32 v162, v158, v159
	s_waitcnt lgkmcnt(1)
	v_mfma_f32_32x32x16_f16 v[34:49], v[154:157], v[150:153], v[34:49]
	v_add_co_u32_e32 v96, vcc, s5, v70
	s_min_u32 s2, s19, 28
	s_nop 0
	v_addc_co_u32_e32 v97, vcc, 0, v71, vcc
	global_store_dwordx4 v[96:97], v[88:91], off nt
	s_add_i32 s21, s17, s2
	s_waitcnt lgkmcnt(0)
	v_mfma_f32_32x32x16_f16 v[34:49], v[162:165], v[66:69], v[34:49]
	ds_read_b128 v[66:69], v191 offset:46080
	v_add_co_u32_e32 v88, vcc, s13, v70
	s_lshl_b32 s2, s21, 13
	s_nop 0
	v_addc_co_u32_e32 v89, vcc, 0, v71, vcc
	global_store_dwordx4 v[88:89], v[92:95], off nt
	ds_read_b128 v[88:91], v191 offset:46112
	s_waitcnt lgkmcnt(1)
	v_mfma_f32_32x32x16_f16 v[18:33], v[154:157], v[66:69], v[18:33]
	v_add_co_u32_e32 v70, vcc, s14, v70
	s_and_b32 s2, s2, 0x3e000
	s_nop 0
	v_addc_co_u32_e32 v71, vcc, 0, v71, vcc
	v_lshl_add_u64 v[66:67], v[170:171], 0, s[2:3]
	v_add_co_u32_e32 v68, vcc, s15, v66
	global_store_dwordx4 v[70:71], v[146:149], off nt
	s_nop 0
	v_addc_co_u32_e32 v69, vcc, 0, v67, vcc
	s_waitcnt lgkmcnt(0)
	v_mfma_f32_32x32x16_f16 v[18:33], v[162:165], v[88:91], v[18:33]
	global_load_dwordx4 v[88:91], v[66:67], off
	global_load_dwordx4 v[92:95], v[68:69], off
	ds_read_b128 v[66:69], v191 offset:50688
	ds_read_b128 v[146:149], v191 offset:50720
	s_min_u32 s2, s19, 29
	s_add_i32 s2, s0, s2
	s_lshl_b32 s2, s2, 7
	s_and_b32 s2, s2, 0xf80
	s_waitcnt lgkmcnt(1)
	v_mfma_f32_32x32x16_f16 v[2:17], v[154:157], v[66:69], v[2:17]
	v_lshl_add_u64 v[66:67], v[172:173], 0, s[2:3]
	v_add_co_u32_e32 v68, vcc, s10, v66
	s_nop 0
	v_addc_co_u32_e32 v69, vcc, 0, v67, vcc
	global_load_dwordx4 v[150:153], v[66:67], off
	global_load_dwordx4 v[154:157], v[68:69], off
	v_mfma_f32_32x32x16_f16 v[72:87], v[198:201], v[134:137], v[72:87]
	v_exp_f32_e32 v97, v98
	s_waitcnt lgkmcnt(0)
	s_barrier
	v_mfma_f32_32x32x16_f16 v[72:87], v[210:213], v[138:141], v[72:87]
	v_mfma_f32_32x32x16_f16 v[72:87], v[166:169], v[142:145], v[72:87]
	v_mfma_f32_32x32x16_f16 v[50:65], v[162:165], v[194:197], v[50:65]
	s_nop 0
	ds_read_b128 v[66:69], v186
	ds_read_b128 v[158:161], v186 offset:32
	ds_read_b128 v[194:197], v186 offset:9216
	ds_read_b128 v[198:201], v186 offset:9248
	ds_read_b128 v[202:205], v186 offset:64
	ds_read_b128 v[206:209], v186 offset:96
	v_exp_f32_e32 v167, v99
	v_exp_f32_e32 v99, v100
	v_exp_f32_e32 v169, v101
	v_exp_f32_e32 v101, v102
	v_mfma_f32_32x32x16_f16 v[2:17], v[162:165], v[146:149], v[2:17]
	ds_read_b128 v[146:149], v186 offset:9280
	ds_read_b128 v[162:165], v186 offset:9312
	v_exp_f32_e32 v211, v103
	v_exp_f32_e32 v103, v104
	v_exp_f32_e32 v213, v105
	v_exp_f32_e32 v105, v106
	v_exp_f32_e32 v215, v107
	v_exp_f32_e32 v107, v108
	v_exp_f32_e32 v217, v109
	v_exp_f32_e32 v166, v72
	v_exp_f32_e32 v96, v73
	v_exp_f32_e32 v168, v74
	v_exp_f32_e32 v98, v75
	v_exp_f32_e32 v210, v76
	v_exp_f32_e32 v100, v77
	v_exp_f32_e32 v212, v78
	v_exp_f32_e32 v102, v79
	v_exp_f32_e32 v214, v80
	v_exp_f32_e32 v104, v81
	s_waitcnt lgkmcnt(7)
	v_mfma_f32_32x32x16_f16 v[66:81], v[66:69], v[114:117], v[240:255]
	v_exp_f32_e32 v109, v110
	v_exp_f32_e32 v216, v82
	v_exp_f32_e32 v106, v83
	v_exp_f32_e32 v219, v111
	s_waitcnt lgkmcnt(6)
	v_mfma_f32_32x32x16_f16 v[66:81], v[158:161], v[118:121], v[66:81]
	v_exp_f32_e32 v218, v84
	v_exp_f32_e32 v108, v85
	v_exp_f32_e32 v111, v112
	v_exp_f32_e32 v110, v87
	s_waitcnt lgkmcnt(3)
	v_mfma_f32_32x32x16_f16 v[66:81], v[202:205], v[122:125], v[66:81]
	v_exp_f32_e32 v202, v86
	v_exp_f32_e32 v203, v113
	s_waitcnt lgkmcnt(2)
	v_mfma_f32_32x32x16_f16 v[66:81], v[206:209], v[126:129], v[66:81]
	s_waitcnt vmcnt(3)
	ds_write_b128 v185, v[88:91] offset:18432
	s_waitcnt vmcnt(2)
	ds_write_b128 v185, v[92:95] offset:27648
	s_waitcnt vmcnt(1)
	ds_write_b128 v185, v[150:153] offset:36864
	s_waitcnt vmcnt(0)
	ds_write_b128 v185, v[154:157] offset:46080
	v_fma_f32 v150, v176, v166, v97
	v_fma_f32 v151, v176, v96, v167
	v_mfma_f32_32x32x16_f16 v[82:97], v[194:197], v[130:133], 0
	v_fma_f32 v152, v176, v168, v99
	v_fma_f32 v153, v176, v98, v169
	v_fma_f32 v154, v176, v210, v101
	v_fma_f32 v155, v176, v100, v211
	v_fma_f32 v156, v176, v212, v103
	v_fma_f32 v157, v176, v102, v213
	v_fma_f32 v158, v176, v214, v105
	v_fma_f32 v159, v176, v104, v215
	v_fma_f32 v160, v176, v216, v107
	v_fma_f32 v161, v176, v106, v217
	v_fma_f32 v166, v176, v218, v109
	v_fma_f32 v167, v176, v108, v219
	v_fma_f32 v168, v176, v202, v111
	v_fma_f32 v169, v176, v110, v203
	ds_read_b128 v[98:101], v189
	ds_read_b128 v[102:105], v189 offset:576
	ds_read_b128 v[106:109], v189 offset:1152
	ds_read_b128 v[110:113], v189 offset:1728
	ds_write_b128 v190, v[150:153] offset:36864
	ds_write_b128 v190, v[154:157] offset:36880
	ds_write_b128 v190, v[158:161] offset:36928
	ds_write_b128 v190, v[166:169] offset:36944
	v_cvt_pk_f16_f32 v157, v156, v157
	v_cvt_pk_f16_f32 v156, v154, v155
	v_cvt_pk_f16_f32 v155, v152, v153
	v_cvt_pk_f16_f32 v154, v150, v151
	ds_read_b128 v[150:153], v191 offset:55296
	ds_read_b128 v[194:197], v191 offset:55328
	v_mfma_f32_32x32x16_f16 v[82:97], v[198:201], v[134:137], v[82:97]
	s_and_b32 s2, s20, 0x7c0
	s_min_u32 s20, s19, 27
	s_lshl_b32 s2, s2, 2
	s_add_i32 s20, s18, s20
	v_lshl_add_u64 v[210:211], v[174:175], 0, s[2:3]
	s_lshl_b32 s2, s20, 13
	s_and_b32 s2, s2, 0x3e000
	s_waitcnt lgkmcnt(1)
	v_mfma_f32_32x32x16_f16 v[50:65], v[154:157], v[150:153], v[50:65]
	ds_read_b128 v[150:153], v191 offset:59904
	ds_read_b128 v[198:201], v191 offset:59936
	s_lshl_b32 s21, s21, 7
	v_cvt_pk_f16_f32 v169, v168, v169
	v_cvt_pk_f16_f32 v168, v166, v167
	v_cvt_pk_f16_f32 v166, v158, v159
	v_cvt_pk_f16_f32 v167, v160, v161
	s_addk_i32 s1, 0x80
	s_waitcnt lgkmcnt(1)
	v_mfma_f32_32x32x16_f16 v[34:49], v[154:157], v[150:153], v[34:49]
	ds_read_b128 v[150:153], v191 offset:64512
	ds_read_b128 v[202:205], v191 offset:64544
	s_waitcnt lgkmcnt(1)
	v_mfma_f32_32x32x16_f16 v[18:33], v[154:157], v[150:153], v[18:33]
	ds_read_b128 v[150:153], v192 offset:13824
	ds_read_b128 v[206:209], v192 offset:13856
	v_mfma_f32_32x32x16_f16 v[82:97], v[146:149], v[138:141], v[82:97]
	v_lshl_add_u64 v[146:147], v[170:171], 0, s[2:3]
	s_and_b32 s2, s21, 0xf80
	v_lshl_add_u64 v[158:159], v[172:173], 0, s[2:3]
	s_add_i32 s2, s19, 2
	s_cmp_lt_u32 s19, 30
	s_mov_b32 s19, s2
	s_waitcnt lgkmcnt(1)
	v_mfma_f32_32x32x16_f16 v[2:17], v[154:157], v[150:153], v[2:17]
	v_add_co_u32_e32 v150, vcc, s15, v146
	s_nop 1
	v_addc_co_u32_e32 v151, vcc, 0, v147, vcc
	global_load_dwordx4 v[146:149], v[146:147], off
	s_nop 0
	global_load_dwordx4 v[150:153], v[150:151], off
	s_nop 0
	global_load_dwordx4 v[154:157], v[158:159], off
	v_add_co_u32_e32 v158, vcc, s10, v158
	v_mfma_f32_32x32x16_f16 v[50:65], v[166:169], v[194:197], v[50:65]
	s_nop 0
	v_addc_co_u32_e32 v159, vcc, 0, v159, vcc
	global_load_dwordx4 v[158:161], v[158:159], off
	v_add_co_u32_e32 v194, vcc, s5, v210
	s_nop 1
	v_addc_co_u32_e32 v195, vcc, 0, v211, vcc
	v_mfma_f32_32x32x16_f16 v[34:49], v[166:169], v[198:201], v[34:49]
	v_add_co_u32_e32 v196, vcc, s13, v210
	s_nop 1
	v_addc_co_u32_e32 v197, vcc, 0, v211, vcc
	v_mfma_f32_32x32x16_f16 v[18:33], v[166:169], v[202:205], v[18:33]
	s_waitcnt lgkmcnt(0)
	v_mfma_f32_32x32x16_f16 v[2:17], v[166:169], v[206:209], v[2:17]
	v_add_co_u32_e32 v166, vcc, s14, v210
	s_nop 1
	v_addc_co_u32_e32 v167, vcc, 0, v211, vcc
	global_store_dwordx4 v[210:211], v[98:101], off nt
	global_store_dwordx4 v[194:195], v[102:105], off nt
	global_store_dwordx4 v[196:197], v[106:109], off nt
	global_store_dwordx4 v[166:167], v[110:113], off nt
	v_mfma_f32_32x32x16_f16 v[82:97], v[162:165], v[142:145], v[82:97]
	s_barrier
	s_cbranch_scc1 .Ll2f_top
.Ll2_post:
	ds_read_b128 v[66:69], v189 offset:36864
	ds_read_b128 v[70:73], v189 offset:37440
	s_addk_i32 s11, 0x7c0
	s_and_b32 s0, s11, 0x7c0
	s_lshl_b32 s0, s0, 2
	s_mov_b32 s1, 0
	v_lshl_add_u64 v[74:75], v[174:175], 0, s[0:1]
	s_waitcnt lgkmcnt(1)
	global_store_dwordx4 v[74:75], v[66:69], off nt
	s_mov_b32 s0, 0x10800
	v_lshlrev_b32_e32 v1, 2, v1
	v_add_co_u32_e32 v66, vcc, 0x8000, v74
	v_lshrrev_b32_e32 v86, 2, v0
	s_nop 0
	v_addc_co_u32_e32 v67, vcc, 0, v75, vcc
	s_waitcnt lgkmcnt(0)
	global_store_dwordx4 v[66:67], v[70:73], off nt
	ds_read_b128 v[66:69], v189 offset:38016
	ds_read_b128 v[70:73], v189 offset:38592
	v_add_co_u32_e32 v76, vcc, 0x10000, v74
	v_lshlrev_b32_e32 v0, 5, v0
	s_nop 0
	v_addc_co_u32_e32 v77, vcc, 0, v75, vcc
	s_waitcnt lgkmcnt(1)
	global_store_dwordx4 v[76:77], v[66:69], off nt
	v_and_b32_e32 v87, 0x60, v0
	v_lshlrev_b32_e32 v88, 2, v87
	v_add_co_u32_e32 v66, vcc, 0x18000, v74
	s_nop 1
	v_addc_co_u32_e32 v67, vcc, 0, v75, vcc
	s_waitcnt lgkmcnt(0)
	global_store_dwordx4 v[66:67], v[70:73], off nt
	v_lshl_or_b32 v67, v182, 2, v183
	v_mad_u32_u24 v66, v184, s0, 0
	v_mul_u32_u24_e32 v67, 0x210, v67
	v_add3_u32 v1, v66, v1, v67
	s_barrier
	ds_write2_b32 v1, v50, v34 offset1:32
	ds_write2_b32 v1, v51, v35 offset0:132 offset1:164
	v_add_u32_e32 v34, 0x400, v1
	ds_write2_b32 v34, v52, v36 offset0:8 offset1:40
	ds_write2_b32 v34, v53, v37 offset0:140 offset1:172
	v_add_u32_e32 v35, 0x1000, v1
	v_add_u32_e32 v36, 0x1400, v1
	ds_write2_b32 v35, v54, v38 offset0:32 offset1:64
	ds_write2_b32 v35, v55, v39 offset0:164 offset1:196
	ds_write2_b32 v36, v56, v40 offset0:40 offset1:72
	ds_write2_b32 v36, v57, v41 offset0:172 offset1:204
	v_add_u32_e32 v37, 0x2000, v1
	v_add_u32_e32 v38, 0x2400, v1
	v_add_u32_e32 v40, 0x3200, v1
	ds_write2_b32 v37, v58, v42 offset0:64 offset1:96
	ds_write2_b32 v37, v59, v43 offset0:196 offset1:228
	ds_write2_b32 v38, v60, v44 offset0:72 offset1:104
	ds_write2_b32 v38, v61, v45 offset0:204 offset1:236
	v_add_u32_e32 v39, 0x3000, v1
	ds_write2_b32 v40, v63, v47 offset0:100 offset1:132
	v_add_u32_e32 v40, 0x3400, v1
	v_add_u32_e32 v41, 0x3600, v1
	ds_write2_b32 v39, v62, v46 offset0:96 offset1:128
	ds_write2_b32 v40, v64, v48 offset0:104 offset1:136
	ds_write2_b32 v41, v65, v49 offset0:108 offset1:140
	ds_write2_b32 v1, v18, v2 offset0:64 offset1:96
	ds_write2_b32 v1, v19, v3 offset0:196 offset1:228
	ds_write2_b32 v34, v20, v4 offset0:72 offset1:104
	ds_write2_b32 v34, v21, v5 offset0:204 offset1:236
	ds_write2_b32 v35, v22, v6 offset0:96 offset1:128
	v_add_u32_e32 v2, 0x1200, v1
	ds_write2_b32 v2, v23, v7 offset0:100 offset1:132
	ds_write2_b32 v36, v24, v8 offset0:104 offset1:136
	v_add_u32_e32 v2, 0x1600, v1
	ds_write2_b32 v2, v25, v9 offset0:108 offset1:140
	ds_write2_b32 v37, v26, v10 offset0:128 offset1:160
	ds_write2_b32 v38, v27, v11 offset0:4 offset1:36
	ds_write2_b32 v38, v28, v12 offset0:136 offset1:168
	v_add_u32_e32 v2, 0x2800, v1
	v_add_u32_e32 v1, 0x3800, v1
	ds_write2_b32 v2, v29, v13 offset0:12 offset1:44
	ds_write2_b32 v39, v30, v14 offset0:160 offset1:192
	ds_write2_b32 v40, v31, v15 offset0:36 offset1:68
	ds_write2_b32 v40, v32, v16 offset0:168 offset1:200
	ds_write2_b32 v1, v33, v17 offset0:44 offset1:76
	v_mul_u32_u24_e32 v1, 0x210, v86
	v_add3_u32 v89, 0, v1, v88
	v_add_u32_e32 v0, 0x10800, v89
	s_waitcnt lgkmcnt(0)
	s_barrier
	ds_read_b128 v[10:13], v0
	ds_read_b128 v[14:17], v0 offset:16
	ds_read_b128 v[4:7], v89 offset:16
	ds_read_b128 v[18:21], v89
	v_add_u32_e32 v26, 0x10820, v89
	ds_read_b128 v[22:25], v89 offset:32
	ds_read_b128 v[0:3], v89 offset:48
	v_add_u32_e32 v34, 0x10810, v89
	s_waitcnt lgkmcnt(3)
	v_pk_add_f32 v[16:17], v[6:7], v[16:17]
	v_pk_add_f32 v[14:15], v[4:5], v[14:15]
	s_waitcnt lgkmcnt(2)
	v_pk_add_f32 v[10:11], v[18:19], v[10:11]
	v_pk_add_f32 v[8:9], v[20:21], v[12:13]
	v_pk_mul_f32 v[20:21], v[16:17], v[16:17]
	v_pk_mul_f32 v[16:17], v[10:11], v[10:11]
	v_pk_mul_f32 v[14:15], v[14:15], v[14:15]
	v_pk_mul_f32 v[12:13], v[8:9], v[8:9]
	v_mov_b32_e32 v18, v16
	v_mov_b32_e32 v19, v14
	v_mov_b32_e32 v14, v17
	v_pk_add_f32 v[14:15], v[18:19], v[14:15]
	v_mov_b32_e32 v16, v12
	v_mov_b32_e32 v17, v20
	v_pk_add_f32 v[18:19], v[14:15], v[16:17]
	v_mov_b32_e32 v20, v13
	ds_read_b128 v[14:17], v26 offset:16
	v_pk_add_f32 v[12:13], v[18:19], v[20:21]
	ds_read_b128 v[18:21], v26
	v_add_u32_e32 v38, 0x10840, v89
	ds_read_b128 v[26:29], v38
	s_waitcnt lgkmcnt(2)
	v_pk_add_f32 v[32:33], v[0:1], v[14:15]
	v_pk_add_f32 v[30:31], v[2:3], v[16:17]
	s_waitcnt lgkmcnt(1)
	v_pk_add_f32 v[80:81], v[22:23], v[18:19]
	v_pk_add_f32 v[78:79], v[24:25], v[20:21]
	v_pk_mul_f32 v[18:19], v[80:81], v[80:81]
	v_pk_mul_f32 v[22:23], v[32:33], v[32:33]
	v_pk_mul_f32 v[20:21], v[78:79], v[78:79]
	v_pk_mul_f32 v[30:31], v[30:31], v[30:31]
	v_mov_b32_e32 v24, v18
	v_mov_b32_e32 v25, v22
	v_mov_b32_e32 v22, v19
	v_pk_add_f32 v[18:19], v[24:25], v[22:23]
	v_mov_b32_e32 v22, v20
	v_mov_b32_e32 v23, v30
	ds_read_b128 v[14:17], v34
	v_pk_add_f32 v[32:33], v[18:19], v[22:23]
	v_mov_b32_e32 v30, v21
	ds_read_b128 v[18:21], v89 offset:80
	ds_read_b128 v[22:25], v38 offset:16
	v_pk_add_f32 v[82:83], v[32:33], v[30:31]
	ds_read_b128 v[30:33], v89 offset:64
	ds_read_b128 v[34:37], v89 offset:80
	ds_read_b128 v[38:41], v38
	ds_read_b128 v[42:45], v89 offset:64
	v_add_u32_e32 v74, 0x10860, v89
	s_waitcnt lgkmcnt(4)
	v_pk_add_f32 v[20:21], v[20:21], v[24:25]
	v_pk_add_f32 v[18:19], v[18:19], v[22:23]
	s_waitcnt lgkmcnt(3)
	v_pk_add_f32 v[22:23], v[30:31], v[26:27]
	v_pk_add_f32 v[24:25], v[32:33], v[28:29]
	v_pk_mul_f32 v[28:29], v[20:21], v[20:21]
	v_pk_mul_f32 v[20:21], v[22:23], v[22:23]
	v_pk_mul_f32 v[30:31], v[18:19], v[18:19]
	v_pk_mul_f32 v[26:27], v[24:25], v[24:25]
	v_mov_b32_e32 v32, v20
	v_mov_b32_e32 v33, v30
	v_mov_b32_e32 v30, v21
	global_load_dwordx4 v[18:21], v88, s[8:9] offset:16
	global_load_dwordx4 v[22:25], v88, s[8:9]
	v_pk_add_f32 v[30:31], v[32:33], v[30:31]
	v_mov_b32_e32 v32, v26
	v_mov_b32_e32 v33, v28
	v_pk_add_f32 v[30:31], v[30:31], v[32:33]
	v_mov_b32_e32 v28, v27
	v_pk_add_f32 v[84:85], v[30:31], v[28:29]
	ds_read_b128 v[26:29], v89 offset:96
	ds_read_b128 v[30:33], v89 offset:112
	ds_read_b128 v[46:49], v74
	ds_read_b128 v[50:53], v74 offset:16
	global_load_dwordx4 v[54:57], v88, s[8:9] offset:48
	global_load_dwordx4 v[58:61], v88, s[8:9] offset:32
	v_add_u32_e32 v62, 0x10830, v89
	ds_read_b128 v[62:65], v62
	ds_read_b128 v[66:69], v89 offset:112
	s_waitcnt lgkmcnt(3)
	v_pk_add_f32 v[28:29], v[28:29], v[48:49]
	s_waitcnt lgkmcnt(2)
	v_pk_add_f32 v[30:31], v[30:31], v[50:51]
	v_pk_add_f32 v[26:27], v[26:27], v[46:47]
	v_pk_mul_f32 v[46:47], v[28:29], v[28:29]
	v_pk_mul_f32 v[26:27], v[26:27], v[26:27]
	v_pk_mul_f32 v[28:29], v[30:31], v[30:31]
	v_pk_add_f32 v[32:33], v[32:33], v[52:53]
	v_mov_b32_e32 v30, v26
	v_mov_b32_e32 v31, v28
	v_mov_b32_e32 v28, v27
	ds_read_b128 v[70:73], v89 offset:96
	ds_read_b128 v[74:77], v74
	v_pk_mul_f32 v[48:49], v[32:33], v[32:33]
	v_pk_add_f32 v[50:51], v[30:31], v[28:29]
	global_load_dwordx4 v[26:29], v88, s[8:9] offset:80
	global_load_dwordx4 v[30:33], v88, s[8:9] offset:64
	v_add_f32_e32 v12, v12, v13
	v_add_f32_e32 v12, v12, v82
	v_mov_b32_e32 v52, v46
	v_mov_b32_e32 v53, v48
	v_add_f32_e32 v12, v12, v83
	v_pk_add_f32 v[50:51], v[50:51], v[52:53]
	v_mov_b32_e32 v48, v47
	v_add_f32_e32 v12, v12, v84
	v_pk_add_f32 v[46:47], v[50:51], v[48:49]
	v_add_f32_e32 v12, v12, v85
	v_add_f32_e32 v12, v12, v46
	v_add_f32_e32 v12, v12, v47
	global_load_dwordx4 v[46:49], v88, s[8:9] offset:96
	global_load_dwordx4 v[50:53], v88, s[8:9] offset:112
	ds_bpermute_b32 v13, v181, v12
	s_mov_b32 s0, 0x800000
	v_pk_add_f32 v[4:5], v[4:5], v[14:15]
	s_waitcnt lgkmcnt(4)
	v_pk_add_f32 v[0:1], v[0:1], v[62:63]
	s_waitcnt lgkmcnt(0)
	v_add_f32_e32 v12, v12, v13
	ds_bpermute_b32 v13, v180, v12
	s_waitcnt lgkmcnt(0)
	v_add_f32_e32 v12, v12, v13
	v_mov_b32_e32 v13, 0x3727c5ac
	v_fmac_f32_e32 v13, 0x3c000000, v12
	v_mul_f32_e32 v12, 0x4b800000, v13
	v_cmp_gt_f32_e32 vcc, s0, v13
	s_lshl_b32 s0, s12, 1
	s_nop 0
	v_cndmask_b32_e32 v12, v13, v12, vcc
	v_rsq_f32_e32 v12, v12
	s_nop 0
	v_mul_f32_e32 v13, 0x45800000, v12
	v_cndmask_b32_e32 v12, v12, v13, vcc
	v_mul_f32_e32 v82, 0x3f4ccccd, v12
	v_add_u32_e32 v12, s16, v86
	v_mov_b32_e32 v13, 0
	v_lshlrev_b64 v[84:85], 12, v[12:13]
	v_lshl_add_u64 v[84:85], s[6:7], 0, v[84:85]
	v_pk_mul_f32 v[4:5], v[82:83], v[4:5] op_sel_hi:[0,1]
	v_lshl_add_u64 v[84:85], v[84:85], 0, s[0:1]
	v_lshlrev_b32_e32 v12, 1, v87
	v_lshl_add_u64 v[84:85], v[84:85], 0, v[12:13]
	v_pk_mul_f32 v[0:1], v[82:83], v[0:1] op_sel_hi:[0,1]
	v_pk_mul_f32 v[10:11], v[82:83], v[10:11] op_sel_hi:[0,1]
	v_pk_mul_f32 v[8:9], v[82:83], v[8:9] op_sel_hi:[0,1]
	s_waitcnt vmcnt(7)
	v_pk_mul_f32 v[4:5], v[4:5], v[18:19]
	s_nop 0
	v_cvt_pk_f16_f32 v12, v4, v5
	v_pk_add_f32 v[4:5], v[6:7], v[16:17]
	v_pk_mul_f32 v[6:7], v[82:83], v[78:79] op_sel_hi:[0,1]
	v_pk_mul_f32 v[4:5], v[82:83], v[4:5] op_sel_hi:[0,1]
	v_pk_mul_f32 v[4:5], v[4:5], v[20:21]
	s_waitcnt vmcnt(6)
	v_pk_mul_f32 v[10:11], v[10:11], v[22:23]
	v_cvt_pk_f16_f32 v13, v4, v5
	v_pk_mul_f32 v[4:5], v[82:83], v[80:81] op_sel_hi:[0,1]
	s_waitcnt vmcnt(4)
	v_pk_mul_f32 v[4:5], v[4:5], v[58:59]
	v_pk_mul_f32 v[6:7], v[6:7], v[60:61]
	v_pk_mul_f32 v[0:1], v[0:1], v[54:55]
	v_cvt_pk_f16_f32 v4, v4, v5
	v_cvt_pk_f16_f32 v5, v6, v7
	v_cvt_pk_f16_f32 v6, v0, v1
	v_pk_add_f32 v[0:1], v[2:3], v[64:65]
	v_pk_add_f32 v[2:3], v[44:45], v[40:41]
	v_pk_mul_f32 v[0:1], v[82:83], v[0:1] op_sel_hi:[0,1]
	v_pk_mul_f32 v[0:1], v[0:1], v[56:57]
	v_pk_mul_f32 v[8:9], v[8:9], v[24:25]
	v_cvt_pk_f16_f32 v7, v0, v1
	global_store_dwordx4 v[84:85], v[4:7], off offset:16
	v_pk_add_f32 v[0:1], v[42:43], v[38:39]
	v_cvt_pk_f16_f32 v10, v10, v11
	v_add_u32_e32 v4, 0x10850, v89
	v_pk_mul_f32 v[6:7], v[82:83], v[2:3] op_sel_hi:[0,1]
	ds_read_b128 v[2:5], v4
	v_pk_mul_f32 v[0:1], v[82:83], v[0:1] op_sel_hi:[0,1]
	s_waitcnt vmcnt(3)
	v_pk_mul_f32 v[0:1], v[0:1], v[30:31]
	v_pk_mul_f32 v[6:7], v[6:7], v[32:33]
	v_cvt_pk_f16_f32 v0, v0, v1
	v_cvt_pk_f16_f32 v1, v6, v7
	v_add_u32_e32 v6, 0x10870, v89
	v_cvt_pk_f16_f32 v11, v8, v9
	ds_read_b128 v[6:9], v6
	s_waitcnt lgkmcnt(1)
	v_pk_add_f32 v[2:3], v[34:35], v[2:3]
	v_pk_add_f32 v[4:5], v[36:37], v[4:5]
	v_pk_mul_f32 v[2:3], v[82:83], v[2:3] op_sel_hi:[0,1]
	v_pk_mul_f32 v[4:5], v[82:83], v[4:5] op_sel_hi:[0,1]
	v_pk_mul_f32 v[2:3], v[2:3], v[26:27]
	v_pk_mul_f32 v[4:5], v[4:5], v[28:29]
	v_cvt_pk_f16_f32 v2, v2, v3
	v_cvt_pk_f16_f32 v3, v4, v5
	global_store_dwordx4 v[84:85], v[0:3], off offset:32
	s_waitcnt lgkmcnt(0)
	v_pk_add_f32 v[4:5], v[68:69], v[8:9]
	global_store_dwordx4 v[84:85], v[10:13], off
	v_pk_add_f32 v[0:1], v[70:71], v[74:75]
	v_pk_add_f32 v[2:3], v[72:73], v[76:77]
	v_pk_mul_f32 v[0:1], v[82:83], v[0:1] op_sel_hi:[0,1]
	v_pk_mul_f32 v[2:3], v[82:83], v[2:3] op_sel_hi:[0,1]
	s_waitcnt vmcnt(4)
	v_pk_mul_f32 v[0:1], v[0:1], v[46:47]
	v_pk_mul_f32 v[2:3], v[2:3], v[48:49]
	v_cvt_pk_f16_f32 v0, v0, v1
	v_cvt_pk_f16_f32 v1, v2, v3
	v_pk_add_f32 v[2:3], v[66:67], v[6:7]
	v_pk_mul_f32 v[4:5], v[82:83], v[4:5] op_sel_hi:[0,1]
	v_pk_mul_f32 v[2:3], v[82:83], v[2:3] op_sel_hi:[0,1]
	s_waitcnt vmcnt(3)
	v_pk_mul_f32 v[2:3], v[2:3], v[50:51]
	v_pk_mul_f32 v[4:5], v[4:5], v[52:53]
	v_cvt_pk_f16_f32 v2, v2, v3
	v_cvt_pk_f16_f32 v3, v4, v5
	global_store_dwordx4 v[84:85], v[0:3], off offset:48
	s_endpgm

	.amdhsa_kernel _Z11attn_kernelPKDF16_S0_PKfS2_S2_S2_S2_PfPDF16_S3_
		.amdhsa_group_segment_fixed_size 8192
		.amdhsa_private_segment_fixed_size 0
		.amdhsa_kernarg_size 80
		.amdhsa_user_sgpr_count 2
		.amdhsa_user_sgpr_dispatch_ptr 0
		.amdhsa_user_sgpr_queue_ptr 0
		.amdhsa_user_sgpr_kernarg_segment_ptr 1
		.amdhsa_user_sgpr_dispatch_id 0
		.amdhsa_user_sgpr_kernarg_preload_length 0
		.amdhsa_user_sgpr_kernarg_preload_offset 0
		.amdhsa_user_sgpr_private_segment_size 0
		.amdhsa_uses_dynamic_stack 0
		.amdhsa_enable_private_segment 0
		.amdhsa_system_sgpr_workgroup_id_x 1
		.amdhsa_system_sgpr_workgroup_id_y 0
		.amdhsa_system_sgpr_workgroup_id_z 0
		.amdhsa_system_sgpr_workgroup_info 0
		.amdhsa_system_vgpr_workitem_id 0
		.amdhsa_next_free_vgpr 256
		.amdhsa_next_free_sgpr 38
		.amdhsa_accum_offset 256
		.amdhsa_reserve_vcc 1
		.amdhsa_float_round_mode_32 0
		.amdhsa_float_round_mode_16_64 0
		.amdhsa_float_denorm_mode_32 3
		.amdhsa_float_denorm_mode_16_64 3
		.amdhsa_dx10_clamp 1
		.amdhsa_ieee_mode 1
		.amdhsa_fp16_overflow 0
		.amdhsa_tg_split 0
		.amdhsa_exception_fp_ieee_invalid_op 0
		.amdhsa_exception_fp_denorm_src 0
		.amdhsa_exception_fp_ieee_div_zero 0
		.amdhsa_exception_fp_ieee_overflow 0
		.amdhsa_exception_fp_ieee_underflow 0
		.amdhsa_exception_fp_ieee_inexact 0
		.amdhsa_exception_int_div_zero 0
	.end_amdhsa_kernel

amdhsa.kernels:
  - .agpr_count:     0
    .args:
      - .actual_access:  read_only
        .address_space:  global
        .offset:         0
        .size:           8
        .value_kind:     global_buffer
      - .actual_access:  write_only
        .address_space:  global
        .offset:         8
        .size:           8
        .value_kind:     global_buffer
    .group_segment_fixed_size: 0
    .kernarg_segment_align: 8
    .kernarg_segment_size: 16
    .language:       OpenCL C
    .language_version:
      - 2
      - 0
    .max_flat_workgroup_size: 256
    .name:           _Z13conv_x_kernelPKfPDF16_
    .private_segment_fixed_size: 0
    .sgpr_count:     14
    .sgpr_spill_count: 0
    .symbol:         _Z13conv_x_kernelPKfPDF16_.kd
    .uniform_work_group_size: 1
    .uses_dynamic_stack: false
    .vgpr_count:     12
    .vgpr_spill_count: 0
    .wavefront_size: 64
  - .agpr_count:     0
    .args:
      - .actual_access:  read_only
        .address_space:  global
        .offset:         0
        .size:           8
        .value_kind:     global_buffer
      - .actual_access:  read_only
        .address_space:  global
        .offset:         8
        .size:           8
        .value_kind:     global_buffer
      - .actual_access:  read_only
        .address_space:  global
        .offset:         16
        .size:           8
        .value_kind:     global_buffer
      - .actual_access:  read_only
        .address_space:  global
        .offset:         24
        .size:           8
        .value_kind:     global_buffer
      - .actual_access:  write_only
        .address_space:  global
        .offset:         32
        .size:           8
        .value_kind:     global_buffer
      - .actual_access:  write_only
        .address_space:  global
        .offset:         40
        .size:           8
        .value_kind:     global_buffer
      - .actual_access:  read_only
        .address_space:  global
        .offset:         48
        .size:           8
        .value_kind:     global_buffer
      - .actual_access:  write_only
        .address_space:  global
        .offset:         56
        .size:           8
        .value_kind:     global_buffer
    .group_segment_fixed_size: 16640
    .kernarg_segment_align: 8
    .kernarg_segment_size: 64
    .language:       OpenCL C
    .language_version:
      - 2
      - 0
    .max_flat_workgroup_size: 256
    .name:           _Z13conv_w_kernelPKfS0_S0_S0_PDF16_S1_S0_S1_
    .private_segment_fixed_size: 0
    .sgpr_count:     26
    .sgpr_spill_count: 0
    .symbol:         _Z13conv_w_kernelPKfS0_S0_S0_PDF16_S1_S0_S1_.kd
    .uniform_work_group_size: 1
    .uses_dynamic_stack: false
    .vgpr_count:     31
    .vgpr_spill_count: 0
    .wavefront_size: 64
  - .agpr_count:     0
    .args:
      - .actual_access:  read_only
        .address_space:  global
        .offset:         0
        .size:           8
        .value_kind:     global_buffer
      - .actual_access:  read_only
        .address_space:  global
        .offset:         8
        .size:           8
        .value_kind:     global_buffer
      - .actual_access:  write_only
        .address_space:  global
        .offset:         16
        .size:           8
        .value_kind:     global_buffer
    .group_segment_fixed_size: 0
    .kernarg_segment_align: 8
    .kernarg_segment_size: 24
    .language:       OpenCL C
    .language_version:
      - 2
      - 0
    .max_flat_workgroup_size: 512
    .name:           _Z9wo_kernelPKDF16_S0_Pf
    .private_segment_fixed_size: 0
    .sgpr_count:     16
    .sgpr_spill_count: 0
    .symbol:         _Z9wo_kernelPKDF16_S0_Pf.kd
    .uniform_work_group_size: 1
    .uses_dynamic_stack: false
    .vgpr_count:     134
    .vgpr_spill_count: 0
    .wavefront_size: 64
  - .agpr_count:     0
    .args:
      - .address_space:  global
        .offset:         0
        .size:           8
        .value_kind:     global_buffer
      - .address_space:  global
        .offset:         8
        .size:           8
        .value_kind:     global_buffer
      - .actual_access:  write_only
        .address_space:  global
        .offset:         16
        .size:           8
        .value_kind:     global_buffer
      - .actual_access:  write_only
        .address_space:  global
        .offset:         24
        .size:           8
        .value_kind:     global_buffer
    .group_segment_fixed_size: 0
    .kernarg_segment_align: 8
    .kernarg_segment_size: 32
    .language:       OpenCL C
    .language_version:
      - 2
      - 0
    .max_flat_workgroup_size: 512
    .name:           _Z10qkv_kernelPKDF16_S0_PDF16_S1_
    .private_segment_fixed_size: 0
    .sgpr_count:     44
    .sgpr_spill_count: 0
    .symbol:         _Z10qkv_kernelPKDF16_S0_PDF16_S1_.kd
    .uniform_work_group_size: 1
    .uses_dynamic_stack: false
    .vgpr_count:     200
    .vgpr_spill_count: 0
    .wavefront_size: 64
  - .agpr_count:     0
    .args:
      - .actual_access:  read_only
        .address_space:  global
        .offset:         0
        .size:           8
        .value_kind:     global_buffer
      - .actual_access:  read_only
        .address_space:  global
        .offset:         8
        .size:           8
        .value_kind:     global_buffer
      - .actual_access:  read_only
        .address_space:  global
        .offset:         16
        .size:           8
        .value_kind:     global_buffer
      - .actual_access:  read_only
        .address_space:  global
        .offset:         24
        .size:           8
        .value_kind:     global_buffer
      - .actual_access:  read_only
        .address_space:  global
        .offset:         32
        .size:           8
        .value_kind:     global_buffer
      - .actual_access:  read_only
        .address_space:  global
        .offset:         40
        .size:           8
        .value_kind:     global_buffer
      - .actual_access:  read_only
        .address_space:  global
        .offset:         48
        .size:           8
        .value_kind:     global_buffer
      - .actual_access:  write_only
        .address_space:  global
        .offset:         56
        .size:           8
        .value_kind:     global_buffer
      - .actual_access:  write_only
        .address_space:  global
        .offset:         64
        .size:           8
        .value_kind:     global_buffer
      - .actual_access:  write_only
        .address_space:  global
        .offset:         72
        .size:           8
        .value_kind:     global_buffer
    .group_segment_fixed_size: 8192
    .kernarg_segment_align: 8
    .kernarg_segment_size: 80
    .language:       OpenCL C
    .language_version:
      - 2
      - 0
    .max_flat_workgroup_size: 512
    .name:           _Z11attn_kernelPKDF16_S0_PKfS2_S2_S2_S2_PfPDF16_S3_
    .private_segment_fixed_size: 0
    .sgpr_count:     44
    .sgpr_spill_count: 0
    .symbol:         _Z11attn_kernelPKDF16_S0_PKfS2_S2_S2_S2_PfPDF16_S3_.kd
    .uniform_work_group_size: 1
    .uses_dynamic_stack: false
    .vgpr_count:     256
    .vgpr_spill_count: 0
    .wavefront_size: 64
